# speedup vs baseline: 1.0525x; 1.0105x over previous
.Lp_q:
	v_lshrrev_b32_e32 v122, 5, v0
	v_lshlrev_b32_e32 v122, 10, v122
	v_and_b32_e32 v125, 31, v0
	v_lshl_add_u32 v122, v125, 4, v122
	s_and_b32 s13, s2, 7
	s_lshl_b32 s14, s13, 14
	v_add_u32_e32 v125, s14, v122
	global_load_dwordx4 v[132:135], v125, s[28:29]
	s_add_i32 s13, s2, 1
	s_and_b32 s13, s13, 7
	s_lshl_b32 s14, s13, 14
	v_add_u32_e32 v125, s14, v122
	global_load_dwordx4 v[136:139], v125, s[28:29]
	s_add_i32 s13, s2, 2
	s_and_b32 s13, s13, 7
	s_lshl_b32 s14, s13, 14
	v_add_u32_e32 v125, s14, v122
	global_load_dwordx4 v[140:143], v125, s[28:29]
	s_add_i32 s13, s2, 3
	s_and_b32 s13, s13, 7
	s_lshl_b32 s14, s13, 14
	v_add_u32_e32 v125, s14, v122
	global_load_dwordx4 v[144:147], v125, s[28:29]
	s_add_i32 s13, s2, 4
	s_and_b32 s13, s13, 7
	s_lshl_b32 s14, s13, 14
	v_add_u32_e32 v125, s14, v122
	global_load_dwordx4 v[148:151], v125, s[28:29]
	s_add_i32 s13, s2, 5
	s_and_b32 s13, s13, 7
	s_lshl_b32 s14, s13, 14
	v_add_u32_e32 v125, s14, v122
	global_load_dwordx4 v[152:155], v125, s[28:29]
	s_add_i32 s13, s2, 6
	s_and_b32 s13, s13, 7
	s_lshl_b32 s14, s13, 14
	v_add_u32_e32 v125, s14, v122
	global_load_dwordx4 v[156:159], v125, s[28:29]
	s_add_i32 s13, s2, 7
	s_and_b32 s13, s13, 7
	s_lshl_b32 s14, s13, 14
	v_add_u32_e32 v125, s14, v122
	global_load_dwordx4 v[160:163], v125, s[28:29]
	s_waitcnt vmcnt(18)
	v_cvt_pk_bf16_f32 v12, v2, v3
	v_cvt_pk_bf16_f32 v13, v4, v5
	ds_write_b64 v124, v[12:13]
	s_waitcnt vmcnt(17)
	v_cvt_pk_bf16_f32 v6, v80, v81
	v_cvt_pk_bf16_f32 v7, v82, v83
	s_and_b32 s13, s2, 7
	s_mul_i32 s14, s13, 0x1100
	v_add_u32_e32 v125, s14, v58
	ds_write_b64 v125, v[6:7]
	s_waitcnt vmcnt(16)
	v_cvt_pk_bf16_f32 v8, v84, v85
	v_cvt_pk_bf16_f32 v9, v86, v87
	s_add_i32 s13, s2, 1
	s_and_b32 s13, s13, 7
	s_mul_i32 s14, s13, 0x1100
	v_add_u32_e32 v10, s14, v58
	ds_write_b64 v10, v[8:9]
	s_waitcnt vmcnt(15)
	v_cvt_pk_bf16_f32 v6, v88, v89
	v_cvt_pk_bf16_f32 v7, v90, v91
	s_add_i32 s13, s2, 2
	s_and_b32 s13, s13, 7
	s_mul_i32 s14, s13, 0x1100
	v_add_u32_e32 v125, s14, v58
	ds_write_b64 v125, v[6:7]
	s_waitcnt vmcnt(14)
	v_cvt_pk_bf16_f32 v8, v92, v93
	v_cvt_pk_bf16_f32 v9, v94, v95
	s_add_i32 s13, s2, 3
	s_and_b32 s13, s13, 7
	s_mul_i32 s14, s13, 0x1100
	v_add_u32_e32 v10, s14, v58
	ds_write_b64 v10, v[8:9]
	s_waitcnt vmcnt(13)
	v_cvt_pk_bf16_f32 v6, v96, v97
	v_cvt_pk_bf16_f32 v7, v98, v99
	s_add_i32 s13, s2, 4
	s_and_b32 s13, s13, 7
	s_mul_i32 s14, s13, 0x1100
	v_add_u32_e32 v125, s14, v58
	ds_write_b64 v125, v[6:7]
	s_waitcnt vmcnt(12)
	v_cvt_pk_bf16_f32 v8, v100, v101
	v_cvt_pk_bf16_f32 v9, v102, v103
	s_add_i32 s13, s2, 5
	s_and_b32 s13, s13, 7
	s_mul_i32 s14, s13, 0x1100
	v_add_u32_e32 v10, s14, v58
	ds_write_b64 v10, v[8:9]
	s_waitcnt vmcnt(11)
	v_cvt_pk_bf16_f32 v6, v108, v109
	v_cvt_pk_bf16_f32 v7, v110, v111
	s_add_i32 s13, s2, 6
	s_and_b32 s13, s13, 7
	s_mul_i32 s14, s13, 0x1100
	v_add_u32_e32 v125, s14, v58
	ds_write_b64 v125, v[6:7]
	s_waitcnt vmcnt(10)
	v_cvt_pk_bf16_f32 v8, v112, v113
	v_cvt_pk_bf16_f32 v9, v114, v115
	s_add_i32 s13, s2, 7
	s_and_b32 s13, s13, 7
	s_mul_i32 s14, s13, 0x1100
	v_add_u32_e32 v10, s14, v58
	ds_write_b64 v10, v[8:9]
	s_waitcnt vmcnt(7)
	v_cvt_pk_bf16_f32 v6, v132, v133
	v_cvt_pk_bf16_f32 v7, v134, v135
	s_and_b32 s13, s2, 7
	s_mul_i32 s14, s13, 0x1100
	s_add_i32 s14, s14, 34816
	v_add_u32_e32 v125, s14, v58
	ds_write_b64 v125, v[6:7]
	s_waitcnt vmcnt(6)
	v_cvt_pk_bf16_f32 v8, v136, v137
	v_cvt_pk_bf16_f32 v9, v138, v139
	s_add_i32 s13, s2, 1
	s_and_b32 s13, s13, 7
	s_mul_i32 s14, s13, 0x1100
	s_add_i32 s14, s14, 34816
	v_add_u32_e32 v10, s14, v58
	ds_write_b64 v10, v[8:9]
	s_waitcnt vmcnt(5)
	v_cvt_pk_bf16_f32 v6, v140, v141
	v_cvt_pk_bf16_f32 v7, v142, v143
	s_add_i32 s13, s2, 2
	s_and_b32 s13, s13, 7
	s_mul_i32 s14, s13, 0x1100
	s_add_i32 s14, s14, 34816
	v_add_u32_e32 v125, s14, v58
	ds_write_b64 v125, v[6:7]
	s_waitcnt vmcnt(4)
	v_cvt_pk_bf16_f32 v8, v144, v145
	v_cvt_pk_bf16_f32 v9, v146, v147
	s_add_i32 s13, s2, 3
	s_and_b32 s13, s13, 7
	s_mul_i32 s14, s13, 0x1100
	s_add_i32 s14, s14, 34816
	v_add_u32_e32 v10, s14, v58
	ds_write_b64 v10, v[8:9]
	s_waitcnt vmcnt(3)
	v_cvt_pk_bf16_f32 v6, v148, v149
	v_cvt_pk_bf16_f32 v7, v150, v151
	s_add_i32 s13, s2, 4
	s_and_b32 s13, s13, 7
	s_mul_i32 s14, s13, 0x1100
	s_add_i32 s14, s14, 34816
	v_add_u32_e32 v125, s14, v58
	ds_write_b64 v125, v[6:7]
	s_waitcnt vmcnt(2)
	v_cvt_pk_bf16_f32 v8, v152, v153
	v_cvt_pk_bf16_f32 v9, v154, v155
	s_add_i32 s13, s2, 5
	s_and_b32 s13, s13, 7
	s_mul_i32 s14, s13, 0x1100
	s_add_i32 s14, s14, 34816
	v_add_u32_e32 v10, s14, v58
	ds_write_b64 v10, v[8:9]
	s_waitcnt vmcnt(1)
	v_cvt_pk_bf16_f32 v6, v156, v157
	v_cvt_pk_bf16_f32 v7, v158, v159
	s_add_i32 s13, s2, 6
	s_and_b32 s13, s13, 7
	s_mul_i32 s14, s13, 0x1100
	s_add_i32 s14, s14, 34816
	v_add_u32_e32 v125, s14, v58
	ds_write_b64 v125, v[6:7]
	s_waitcnt vmcnt(0)
	v_cvt_pk_bf16_f32 v8, v160, v161
	v_cvt_pk_bf16_f32 v9, v162, v163
	s_add_i32 s13, s2, 7
	s_and_b32 s13, s13, 7
	s_mul_i32 s14, s13, 0x1100
	s_add_i32 s14, s14, 34816
	v_add_u32_e32 v10, s14, v58
	ds_write_b64 v10, v[8:9]
	v_lshl_add_u32 v123, v128, 1, s12
	v_lshlrev_b32_e32 v123, 12, v123
	v_lshl_add_u32 v123, v126, 4, v123
	v_add_u32_e32 v125, 0x1000, v123
	global_load_dwordx4 v[2:5], v123, s[34:35] nt
	global_load_dwordx4 v[6:9], v123, s[34:35] offset:1024 nt
	global_load_dwordx4 v[10:13], v123, s[34:35] offset:2048 nt
	global_load_dwordx4 v[14:17], v123, s[34:35] offset:3072 nt
	global_load_dwordx4 v[132:135], v125, s[34:35] nt
	global_load_dwordx4 v[136:139], v125, s[34:35] offset:1024 nt
	global_load_dwordx4 v[140:143], v125, s[34:35] offset:2048 nt
	global_load_dwordx4 v[144:147], v125, s[34:35] offset:3072 nt
	s_waitcnt lgkmcnt(0)
	s_barrier
	ds_read_b128 v[28:31], v53
	ds_read_b128 v[60:63], v56
	ds_read_b128 v[32:35], v53 offset:64
	ds_read_b128 v[64:67], v56 offset:64
	ds_read_b128 v[36:39], v53 offset:128
	ds_read_b128 v[68:71], v56 offset:128
	ds_read_b128 v[40:43], v53 offset:192
	ds_read_b128 v[72:75], v56 offset:192
	s_waitcnt lgkmcnt(6)
	v_mfma_f32_16x16x32_bf16 v[18:21], v[28:31], v[60:63], 0
	s_waitcnt lgkmcnt(4)
	v_mfma_f32_16x16x32_bf16 v[18:21], v[32:35], v[64:67], v[18:21]
	s_waitcnt lgkmcnt(2)
	v_mfma_f32_16x16x32_bf16 v[18:21], v[36:39], v[68:71], v[18:21]
	s_waitcnt lgkmcnt(0)
	v_mfma_f32_16x16x32_bf16 v[18:21], v[40:43], v[72:75], v[18:21]
	s_nop 7
	v_mul_f32_e32 v18, s44, v18
	v_mul_f32_e32 v19, s44, v19
	v_mul_f32_e32 v20, s44, v20
	v_mul_f32_e32 v21, s44, v21
	v_cvt_pk_bf16_f32 v18, v18, v18
	v_cvt_pk_bf16_f32 v19, v19, v19
	v_cvt_pk_bf16_f32 v20, v20, v20
	v_cvt_pk_bf16_f32 v21, v21, v21
	ds_write_b16 v55, v18
	ds_write_b16 v55, v19 offset:272
	ds_write_b16 v55, v20 offset:544
	ds_write_b16 v55, v21 offset:816
	s_waitcnt lgkmcnt(0)
	s_barrier
	ds_read_b128 v[28:31], v54
	ds_read_b128 v[60:63], v57
	ds_read_b128 v[32:35], v54 offset:64
	ds_read_b128 v[64:67], v57 offset:64
	ds_read_b128 v[36:39], v54 offset:128
	ds_read_b128 v[68:71], v57 offset:128
	ds_read_b128 v[40:43], v54 offset:192
	ds_read_b128 v[72:75], v57 offset:192
	s_waitcnt lgkmcnt(6)
	v_mfma_f32_16x16x32_bf16 v[18:21], v[28:31], v[60:63], 0
	s_waitcnt lgkmcnt(4)
	v_mfma_f32_16x16x32_bf16 v[18:21], v[32:35], v[64:67], v[18:21]
	s_waitcnt lgkmcnt(2)
	v_mfma_f32_16x16x32_bf16 v[18:21], v[36:39], v[68:71], v[18:21]
	s_waitcnt lgkmcnt(0)
	v_mfma_f32_16x16x32_bf16 v[18:21], v[40:43], v[72:75], v[18:21]
	s_load_dwordx2 s[4:5], s[0:1], 0x68
	v_lshl_or_b32 v26, v24, 2, s12
	v_mov_b32_e32 v107, 0
	v_ashrrev_i32_e32 v27, 31, v26
	v_lshlrev_b64 v[28:29], 9, v[26:27]
	s_waitcnt lgkmcnt(0)
	v_lshl_add_u64 v[30:31], s[4:5], 0, v[106:107]
	v_lshl_add_u64 v[28:29], v[30:31], 0, v[28:29]
	v_mul_u32_u24_e32 v24, 0x440, v24
	s_mov_b32 s4, 0x19200
	global_store_dword v[28:29], v18, off sc1
	v_add3_u32 v28, v24, v25, s4
	v_mul_f32_e32 v24, v18, v18
	v_cvt_pk_bf16_f32 v27, v18, s0
	v_cvt_pk_bf16_f32 v24, v24, s0
	ds_write_b16 v28, v27
	ds_write_b16 v28, v24 offset:4352
	v_max3_f32 v27, |v18|, 0, |v19|
	v_or_b32_e32 v24, 1, v26
	v_cvt_pk_bf16_f32 v18, v19, s0
	v_ashrrev_i32_e32 v25, 31, v24
	ds_write_b16 v28, v18 offset:272
	v_mul_f32_e32 v18, v19, v19
	v_lshlrev_b64 v[24:25], 9, v[24:25]
	v_cvt_pk_bf16_f32 v18, v18, s0
	v_lshl_add_u64 v[24:25], v[30:31], 0, v[24:25]
	ds_write_b16 v28, v18 offset:4624
	v_or_b32_e32 v18, 2, v26
	global_store_dword v[24:25], v19, off sc1
	v_ashrrev_i32_e32 v19, 31, v18
	v_lshlrev_b64 v[18:19], 9, v[18:19]
	v_lshl_add_u64 v[18:19], v[30:31], 0, v[18:19]
	global_store_dword v[18:19], v20, off sc1
	v_cvt_pk_bf16_f32 v18, v20, s0
	ds_write_b16 v28, v18 offset:544
	v_mul_f32_e32 v18, v20, v20
	v_cvt_pk_bf16_f32 v18, v18, s0
	ds_write_b16 v28, v18 offset:4896
	v_or_b32_e32 v18, 3, v26
	v_ashrrev_i32_e32 v19, 31, v18
	v_lshlrev_b64 v[18:19], 9, v[18:19]
	v_lshl_add_u64 v[18:19], v[30:31], 0, v[18:19]
	global_store_dword v[18:19], v21, off sc1
	v_cvt_pk_bf16_f32 v18, v21, s0
	ds_write_b16 v28, v18 offset:816
	v_mul_f32_e32 v18, v21, v21
	v_cvt_pk_bf16_f32 v18, v18, s0
	v_max3_f32 v20, v27, |v20|, |v21|
	ds_write_b16 v28, v18 offset:5168
	v_mov_b32_e32 v18, v107
	v_mov_b32_e32 v19, v107
	v_cmp_eq_u32_e32 vcc, 0, v126
	v_mov_b32_dpp v18, v20 quad_perm:[1,0,3,2] row_mask:0xf bank_mask:0xf
	v_max_f32_e32 v18, v18, v18
	v_max_f32_e32 v18, v20, v18
	s_nop 1
	v_mov_b32_dpp v19, v18 quad_perm:[2,3,0,1] row_mask:0xf bank_mask:0xf
	v_max_f32_e32 v19, v19, v19
	v_max_f32_e32 v18, v18, v19
	v_mov_b32_e32 v19, v107
	s_nop 1
	v_mov_b32_dpp v19, v18 row_half_mirror row_mask:0xf bank_mask:0xf
	v_max_f32_e32 v19, v19, v19
	v_max_f32_e32 v18, v18, v19
	v_mov_b32_e32 v19, v107
	s_nop 1
	v_mov_b32_dpp v19, v18 row_mirror row_mask:0xf bank_mask:0xf
	v_max_f32_e32 v19, v19, v19
	v_max_f32_e32 v18, v18, v19
	s_nop 0
	v_readlane_b32 s8, v18, 0
	v_readlane_b32 s9, v18, 16
	v_readlane_b32 s10, v18, 32
	v_readlane_b32 s11, v18, 48
	v_and_b32_e32 v18, 0x7fffffff, v129
	s_nop 1
	v_add_f32_dpp v18, v18, |v129| quad_perm:[1,0,3,2] row_mask:0xf bank_mask:0xf bound_ctrl:1
	s_nop 1
	v_add_f32_dpp v18, v18, v18 quad_perm:[2,3,0,1] row_mask:0xf bank_mask:0xf bound_ctrl:1
	s_nop 1
	v_add_f32_dpp v18, v18, v18 row_half_mirror row_mask:0xf bank_mask:0xf bound_ctrl:1
	s_nop 1
	v_mov_b32_dpp v107, v18 row_mirror row_mask:0xf bank_mask:0xf
	s_and_saveexec_b64 s[4:5], vcc
	s_cbranch_execz .LBB0_27
	v_mov_b32_e32 v19, 0x1d800
	v_lshl_or_b32 v20, v128, 6, v19
	v_add_f32_e32 v19, v18, v107
	v_max_f32_e64 v18, s11, s11
	v_max_f32_e64 v21, s10, s10
	v_max_f32_e32 v18, v21, v18
	v_mov_b32_e32 v21, s9
	v_max3_f32 v18, s8, v21, v18
	ds_write_b64 v20, v[18:19]
